# baseline (speedup 1.0000x reference)
.LBB2_15:
	s_or_b64 exec, exec, s[6:7]
	v_mov_b32_e32 v12, 1
	s_waitcnt lgkmcnt(0)
	s_barrier
	ds_read_b32 v13, v5 offset:2048
	ds_add_rtn_u32 v17, v5, v12 offset:1024
	ds_read_b32 v14, v7 offset:2048
	ds_add_rtn_u32 v18, v7, v12 offset:1024
	ds_read_b32 v15, v8 offset:2048
	ds_add_rtn_u32 v19, v8, v12 offset:1024
	ds_read_b32 v16, v6 offset:2048
	ds_add_rtn_u32 v20, v6, v12 offset:1024
	s_movk_i32 s0, 0xc8
	v_cmp_gt_u32_e32 vcc, s0, v0
	s_waitcnt lgkmcnt(6)
	v_add_u32_e32 v10, v17, v13
	v_ashrrev_i32_e32 v11, 31, v10
	v_lshl_add_u64 v[10:11], v[10:11], 2, s[2:3]
	global_store_dword v[10:11], v0, off
	s_waitcnt lgkmcnt(4)
	v_add_u32_e32 v10, v18, v14
	v_ashrrev_i32_e32 v11, 31, v10
	v_lshl_add_u64 v[10:11], v[10:11], 2, s[2:3]
	global_store_dword v[10:11], v1, off
	s_waitcnt lgkmcnt(2)
	v_add_u32_e32 v8, v19, v15
	v_ashrrev_i32_e32 v9, 31, v8
	v_lshl_add_u64 v[8:9], v[8:9], 2, s[2:3]
	global_store_dword v[8:9], v2, off
	s_waitcnt lgkmcnt(0)
	v_add_u32_e32 v6, v20, v16
	v_ashrrev_i32_e32 v7, 31, v6
	v_lshl_add_u64 v[6:7], v[6:7], 2, s[2:3]
	global_store_dword v[6:7], v3, off
	s_and_saveexec_b64 s[0:1], vcc
	s_cbranch_execz .LBB2_24
	v_cmp_lt_i32_e32 vcc, 0, v4
	s_and_b64 exec, exec, vcc
	s_cbranch_execz .LBB2_24
	v_lshlrev_b32_e32 v1, 2, v0
	ds_read2st64_b32 v[6:7], v1 offset0:8 offset1:12
	v_add_u32_e32 v1, -1, v4
	v_lshrrev_b32_e32 v1, 5, v1
	s_mov_b32 s6, 1
	v_add_u32_e32 v13, 1, v1
	s_mov_b32 s7, 32
	v_cmp_lt_u32_e32 vcc, 32, v4
	s_mov_b64 s[2:3], -1
	v_mov_b32_e32 v8, 0
	v_mov_b32_e32 v5, 0
	s_and_saveexec_b64 s[0:1], vcc
	s_cbranch_execz .LBB2_21
	v_and_b32_e32 v8, 0xffffffe, v13
	s_waitcnt lgkmcnt(0)
	v_mov_b32_e32 v10, v6
	v_mov_b32_e32 v5, v6
	v_mov_b32_e32 v9, v4
	v_mov_b32_e32 v12, v7
	v_mov_b32_e32 v11, v7
	s_mov_b32 s8, 0
	s_mov_b64 s[2:3], 0
	v_mov_b32_e32 v3, 0
	v_mov_b32_e32 v14, v8
	s_mov_b32 s9, 0
